# P5 mLSTM-output units: the 12 K/V staging loads of a unit issued together into dead registers and written to LDS behind counted waits (hipcc had serialized them: load, vmcnt(0), ds_write, 12 times)
# speedup vs baseline: 1.0067x; 1.0049x over previous
.LBB0_759:
	s_ashr_i32 s54, s52, 8
	s_ashr_i32 s55, s54, 31
	s_lshl_b32 s53, s52, 7
	s_ashr_i32 vcc_lo, s52, 6
	s_lshl_b64 s[58:59], s[54:55], 13
	s_and_b32 s96, s53, 0x1f80
	s_and_b32 s49, vcc_lo, 3
	s_or_b32 s54, s58, s96
	s_mov_b32 s55, s59
	s_lshl_b32 s56, s49, 8
	s_mov_b32 s57, s97
	v_lshl_add_u64 v[0:1], s[54:55], 0, v[92:93]
	v_lshl_add_u64 v[4:5], v[90:91], 0, s[56:57]
	v_lshlrev_b64 v[0:1], 10, v[0:1]
	v_lshl_add_u64 v[0:1], v[4:5], 0, v[0:1]
	global_load_dwordx4 v[52:55], v[0:1], off
	s_lshl_b32 s53, s49, 9
	s_add_u32 s60, s88, s53
	s_addc_u32 s61, s89, 0
	v_mov_b32_e32 v137, v85
	s_ashr_i32 s53, s52, 31
	v_lshl_add_u64 v[0:1], s[54:55], 0, v[94:95]
	v_lshlrev_b64 v[0:1], 10, v[0:1]
	v_lshl_add_u64 v[0:1], v[4:5], 0, v[0:1]
	global_load_dwordx4 v[8:11], v[0:1], off
	v_lshl_add_u64 v[0:1], s[54:55], 0, v[96:97]
	v_lshlrev_b64 v[0:1], 10, v[0:1]
	v_lshl_add_u64 v[0:1], v[4:5], 0, v[0:1]
	global_load_dwordx4 v[12:15], v[0:1], off
	v_lshl_add_u64 v[0:1], s[54:55], 0, v[98:99]
	v_lshlrev_b64 v[0:1], 10, v[0:1]
	v_lshl_add_u64 v[0:1], v[4:5], 0, v[0:1]
	global_load_dwordx4 v[16:19], v[0:1], off
	v_lshl_add_u64 v[0:1], s[60:61], 0, v[136:137]
	s_mov_b64 s[60:61], 0x1200
	v_lshl_add_u64 v[4:5], v[0:1], 0, s[60:61]
	v_lshl_add_u64 v[0:1], s[54:55], 0, v[100:101]
	v_mad_u64_u32 v[2:3], s[60:61], v0, s65, v[4:5]
	v_mad_i32_i24 v3, v1, s65, v3
	global_load_dwordx4 v[20:23], v[2:3], off
	v_lshl_add_u64 v[0:1], s[54:55], 0, v[102:103]
	v_mad_u64_u32 v[2:3], s[60:61], v0, s65, v[4:5]
	v_mad_i32_i24 v3, v1, s65, v3
	global_load_dwordx4 v[24:27], v[2:3], off
	v_lshl_add_u64 v[0:1], s[54:55], 0, v[104:105]
	v_mad_u64_u32 v[2:3], s[60:61], v0, s65, v[4:5]
	v_mad_i32_i24 v3, v1, s65, v3
	global_load_dwordx4 v[28:31], v[2:3], off
	v_lshl_add_u64 v[0:1], s[54:55], 0, v[106:107]
	v_mad_u64_u32 v[2:3], s[60:61], v0, s65, v[4:5]
	v_mad_i32_i24 v3, v1, s65, v3
	global_load_dwordx4 v[32:35], v[2:3], off
	v_lshl_add_u64 v[0:1], s[54:55], 0, v[108:109]
	v_mad_u64_u32 v[2:3], s[60:61], v0, s65, v[4:5]
	v_mad_i32_i24 v3, v1, s65, v3
	global_load_dwordx4 v[36:39], v[2:3], off
	v_lshl_add_u64 v[0:1], s[54:55], 0, v[110:111]
	v_mad_u64_u32 v[2:3], s[60:61], v0, s65, v[4:5]
	v_mad_i32_i24 v3, v1, s65, v3
	global_load_dwordx4 v[40:43], v[2:3], off
	v_lshl_add_u64 v[0:1], s[54:55], 0, v[112:113]
	v_mad_u64_u32 v[2:3], s[60:61], v0, s65, v[4:5]
	v_mad_i32_i24 v3, v1, s65, v3
	global_load_dwordx4 v[44:47], v[2:3], off
	v_lshl_add_u64 v[0:1], s[54:55], 0, v[114:115]
	v_mad_u64_u32 v[2:3], s[60:61], v0, s65, v[4:5]
	v_mad_i32_i24 v3, v1, s65, v3
	global_load_dwordx4 v[48:51], v[2:3], off
	s_lshl_b64 s[60:61], s[52:53], 2
	s_add_u32 s60, s33, s60
	s_addc_u32 s61, s62, s61
	s_waitcnt vmcnt(11)
	ds_write_b128 v182, v[52:55]
	s_waitcnt vmcnt(10)
	ds_write_b128 v183, v[8:11]
	s_waitcnt vmcnt(9)
	ds_write_b128 v184, v[12:15]
	s_waitcnt vmcnt(8)
	ds_write_b128 v185, v[16:19]
	s_waitcnt vmcnt(7)
	ds_write_b128 v186, v[20:23] offset:34816
	s_waitcnt vmcnt(6)
	ds_write_b128 v187, v[24:27] offset:34816
	s_waitcnt vmcnt(5)
	ds_write_b128 v188, v[28:31] offset:34816
	s_waitcnt vmcnt(4)
	ds_write_b128 v189, v[32:35] offset:34816
	s_waitcnt vmcnt(3)
	ds_write_b128 v190, v[36:39] offset:34816
	s_waitcnt vmcnt(2)
	ds_write_b128 v191, v[40:43] offset:34816
	s_waitcnt vmcnt(1)
	ds_write_b128 v192, v[44:47] offset:34816
	s_waitcnt vmcnt(0)
	ds_write_b128 v193, v[48:51] offset:34816
	global_load_dword v0, v85, s[60:61]
	v_mov_b32_e32 v2, 0xff800000
	v_mov_b32_e32 v1, v85
	s_and_saveexec_b64 s[60:61], s[16:17]
	s_cbranch_execz .LBB0_761
	s_ashr_i32 vcc_hi, vcc_lo, 31
	s_lshl_b64 s[74:75], vcc, 13
	s_or_b64 s[74:75], s[74:75], s[96:97]
	v_lshl_add_u64 v[2:3], s[74:75], 0, v[88:89]
	v_lshlrev_b64 v[2:3], 2, v[2:3]
	v_lshl_add_u64 v[4:5], s[44:45], 0, v[2:3]
	v_lshl_add_u64 v[2:3], s[46:47], 0, v[2:3]
	s_lshl_b64 s[74:75], s[52:53], 9
	global_load_dword v1, v[4:5], off
	s_nop 0
	global_load_dword v2, v[2:3], off
	v_lshl_add_u64 v[4:5], v[128:129], 0, s[74:75]
	global_load_dword v3, v[4:5], off
	s_waitcnt vmcnt(1)
	v_sub_f32_e32 v2, v2, v1
	s_waitcnt vmcnt(0)
	ds_write_b32 v168, v3
